# k_final: output stores written through (sc1)
# speedup vs baseline: 1.0644x; 1.0062x over previous
.LBB1_37:
	v_lshrrev_b32_e32 v18, 5, v1
	s_mulk_i32 s20, 0x4100
	v_mul_u32_u24_e32 v18, 0x410, v18
	v_lshlrev_b32_e32 v19, 2, v143
	v_add3_u32 v18, s20, v18, v19
	v_add_u32_e32 v19, 0x800, v18
	s_nop 0
	ds_write2_b32 v18, v50, v66 offset1:32
	ds_write2_b32 v18, v51, v67 offset0:65 offset1:97
	ds_write2_b32 v18, v52, v68 offset0:130 offset1:162
	ds_write2_b32 v18, v53, v69 offset0:195 offset1:227
	ds_write2_b32 v19, v54, v70 offset0:8 offset1:40
	ds_write2_b32 v19, v55, v71 offset0:73 offset1:105
	ds_write2_b32 v19, v56, v72 offset0:138 offset1:170
	ds_write2_b32 v19, v57, v73 offset0:203 offset1:235
	v_add_u32_e32 v19, 0x1000, v18
	ds_write2_b32 v19, v58, v74 offset0:16 offset1:48
	ds_write2_b32 v19, v59, v75 offset0:81 offset1:113
	ds_write2_b32 v19, v60, v76 offset0:146 offset1:178
	ds_write2_b32 v19, v61, v77 offset0:211 offset1:243
	v_add_u32_e32 v19, 0x1800, v18
	ds_write2_b32 v19, v62, v78 offset0:24 offset1:56
	ds_write2_b32 v19, v63, v79 offset0:89 offset1:121
	ds_write2_b32 v19, v64, v80 offset0:154 offset1:186
	ds_write2_b32 v19, v65, v81 offset0:219 offset1:251
	v_add_u32_e32 v19, 0x2000, v18
	ds_write2_b32 v19, v34, v2 offset0:32 offset1:64
	ds_write2_b32 v19, v35, v3 offset0:97 offset1:129
	ds_write2_b32 v19, v36, v4 offset0:162 offset1:194
	v_add_u32_e32 v2, 0x2200, v18
	ds_write2_b32 v2, v37, v5 offset0:99 offset1:131
	v_add_u32_e32 v2, 0x2800, v18
	ds_write2_b32 v2, v38, v6 offset0:40 offset1:72
	ds_write2_b32 v2, v39, v7 offset0:105 offset1:137
	ds_write2_b32 v2, v40, v8 offset0:170 offset1:202
	v_add_u32_e32 v2, 0x2a00, v18
	ds_write2_b32 v2, v41, v9 offset0:107 offset1:139
	v_add_u32_e32 v2, 0x3000, v18
	ds_write2_b32 v2, v42, v10 offset0:48 offset1:80
	ds_write2_b32 v2, v43, v11 offset0:113 offset1:145
	ds_write2_b32 v2, v44, v12 offset0:178 offset1:210
	v_add_u32_e32 v2, 0x3200, v18
	v_lshrrev_b32_e32 v4, 4, v0
	ds_write2_b32 v2, v45, v13 offset0:115 offset1:147
	v_add_u32_e32 v2, 0x3800, v18
	s_waitcnt vmcnt(3)
	v_and_b32_e32 v20, 28, v4
	s_movk_i32 s0, 0x104
	ds_write2_b32 v2, v46, v14 offset0:56 offset1:88
	ds_write2_b32 v2, v47, v15 offset0:121 offset1:153
	ds_write2_b32 v2, v48, v16 offset0:186 offset1:218
	v_add_u32_e32 v2, 0x3a00, v18
	v_mad_u32_u24 v21, v1, s0, v20
	ds_write2_b32 v2, v49, v17 offset0:123 offset1:155
	s_waitcnt lgkmcnt(0)
	s_barrier
	ds_read2_b32 v[4:5], v21 offset1:32
	v_add_u32_e32 v6, 0x4000, v21
	ds_read2_b32 v[6:7], v6 offset0:64 offset1:96
	v_add_u32_e32 v8, 0x8000, v21
	ds_read2_b32 v[8:9], v8 offset0:128 offset1:160
	v_add_u32_e32 v10, 0xc000, v21
	ds_read2_b32 v[10:11], v10 offset0:192 offset1:224
	s_waitcnt lgkmcnt(3)
	v_add_f32_e32 v4, 0, v4
	s_waitcnt lgkmcnt(2)
	v_add_f32_e32 v4, v4, v6
	s_waitcnt lgkmcnt(1)
	v_add_f32_e32 v4, v4, v8
	v_add_u32_e32 v6, 0x10400, v21
	s_waitcnt lgkmcnt(0)
	v_add_f32_e32 v4, v4, v10
	v_add_u32_e32 v8, 0x14500, v21
	v_add_u32_e32 v10, 0x18600, v21
	v_add_u32_e32 v12, 0x1c700, v21
	ds_read_b32 v6, v6
	ds_read_b32 v8, v8
	ds_read_b32 v10, v10
	ds_read_b32 v12, v12
	ds_read_b32 v22, v21 offset:192
	ds_read_b32 v23, v21 offset:16832
	s_waitcnt lgkmcnt(5)
	v_add_f32_e32 v4, v4, v6
	s_waitcnt lgkmcnt(4)
	v_add_f32_e32 v4, v4, v8
	s_waitcnt lgkmcnt(3)
	v_add_f32_e32 v4, v4, v10
	v_lshrrev_b32_e32 v10, 4, v142
	v_and_b32_e32 v10, 0xffffffc, v10
	v_mad_u32_u24 v15, v1, s0, v10
	v_or_b32_e32 v6, 0x23900, v20
	v_or_b32_e32 v8, 0x23800, v20
	v_add_u32_e32 v14, 0x14500, v15
	v_add_u32_e32 v16, 0x18600, v15
	v_add_u32_e32 v17, 0x1c700, v15
	s_waitcnt lgkmcnt(2)
	v_add_f32_e32 v4, v4, v12
	v_add_u32_e32 v13, 0x10400, v15
	v_add_u32_e32 v18, 0x23900, v10
	v_add_u32_e32 v10, 0x23800, v10
	ds_read_b32 v6, v6
	ds_read_b32 v12, v8
	ds_read_b32 v8, v13
	s_waitcnt vmcnt(2)
	ds_read_b32 v24, v14
	ds_read_b32 v25, v16
	ds_read_b32 v26, v17
	ds_read_b32 v27, v18
	ds_read_b32 v14, v10
	ds_read2st64_b32 v[16:17], v15 offset1:65
	s_mov_b32 s9, 0
	s_waitcnt lgkmcnt(7)
	v_ashrrev_i32_e32 v13, 31, v12
	v_lshlrev_b32_e32 v2, 2, v1
	v_mov_b32_e32 v3, 0
	v_lshl_add_u64 v[12:13], v[12:13], 0, s[8:9]
	ds_read2st64_b32 v[18:19], v15 offset0:130 offset1:195
	v_lshl_add_u64 v[2:3], s[10:11], 0, v[2:3]
	v_lshlrev_b64 v[12:13], 8, v[12:13]
	v_mul_f32_e32 v4, v4, v6
	v_lshl_add_u64 v[12:13], v[2:3], 0, v[12:13]
	global_store_dword v[12:13], v4, off sc1
	s_waitcnt lgkmcnt(1)
	v_add_f32_e32 v4, 0, v16
	v_add_f32_e32 v4, v4, v17
	s_waitcnt lgkmcnt(0)
	v_add_f32_e32 v4, v4, v18
	v_lshrrev_b32_e32 v6, 4, v141
	v_add_f32_e32 v4, v4, v19
	v_and_b32_e32 v6, 0xffffffc, v6
	v_add_f32_e32 v4, v4, v8
	v_ashrrev_i32_e32 v15, 31, v14
	v_mad_u32_u24 v8, v1, s0, v6
	v_lshl_add_u64 v[12:13], v[14:15], 0, s[8:9]
	ds_read2st64_b32 v[14:15], v8 offset1:65
	v_add_f32_e32 v4, v4, v24
	v_add_f32_e32 v4, v4, v25
	ds_read2st64_b32 v[16:17], v8 offset0:130 offset1:195
	v_add_f32_e32 v4, v4, v26
	v_lshlrev_b64 v[12:13], 8, v[12:13]
	v_mul_f32_e32 v4, v4, v27
	v_lshl_add_u64 v[12:13], v[2:3], 0, v[12:13]
	global_store_dword v[12:13], v4, off sc1
	s_waitcnt lgkmcnt(1)
	v_add_f32_e32 v4, 0, v14
	v_add_f32_e32 v4, v4, v15
	v_lshrrev_b32_e32 v15, 4, v140
	s_waitcnt lgkmcnt(0)
	v_add_f32_e32 v4, v4, v16
	v_and_b32_e32 v18, 0xffffffc, v15
	v_add_f32_e32 v4, v4, v17
	v_add_u32_e32 v10, 0x10400, v8
	v_add_u32_e32 v12, 0x14500, v8
	v_add_u32_e32 v13, 0x18600, v8
	v_add_u32_e32 v8, 0x1c700, v8
	v_add_u32_e32 v14, 0x23900, v6
	v_add_u32_e32 v6, 0x23800, v6
	v_mad_u32_u24 v19, v1, s0, v18
	v_add_u32_e32 v15, 0x10400, v19
	v_add_u32_e32 v16, 0x14500, v19
	ds_read_b32 v10, v10
	ds_read_b32 v17, v12
	ds_read_b32 v13, v13
	ds_read_b32 v8, v8
	ds_read_b32 v14, v14
	ds_read_b32 v12, v6
	ds_read_b32 v6, v15
	ds_read_b32 v24, v16
	s_waitcnt lgkmcnt(7)
	v_add_f32_e32 v4, v4, v10
	s_waitcnt lgkmcnt(6)
	v_add_f32_e32 v4, v4, v17
	s_waitcnt lgkmcnt(5)
	v_add_f32_e32 v4, v4, v13
	s_waitcnt lgkmcnt(4)
	v_add_f32_e32 v4, v4, v8
	s_waitcnt lgkmcnt(3)
	v_mul_f32_e32 v4, v4, v14
	ds_read2st64_b32 v[14:15], v19 offset1:65
	s_waitcnt lgkmcnt(3)
	v_ashrrev_i32_e32 v13, 31, v12
	v_lshl_add_u64 v[12:13], v[12:13], 0, s[8:9]
	ds_read2st64_b32 v[16:17], v19 offset0:130 offset1:195
	v_lshlrev_b64 v[12:13], 8, v[12:13]
	v_lshl_add_u64 v[12:13], v[2:3], 0, v[12:13]
	global_store_dword v[12:13], v4, off sc1
	s_waitcnt lgkmcnt(1)
	v_add_f32_e32 v4, 0, v14
	v_add_f32_e32 v4, v4, v15
	s_waitcnt lgkmcnt(0)
	v_add_f32_e32 v4, v4, v16
	v_add_f32_e32 v4, v4, v17
	v_add_f32_e32 v4, v4, v6
	v_add_u32_e32 v6, 0x18600, v19
	v_add_u32_e32 v8, 0x1c700, v19
	v_add_u32_e32 v10, 0x23900, v18
	v_add_u32_e32 v12, 0x23800, v18
	v_add_u32_e32 v14, 0x14580, v21
	v_add_u32_e32 v15, 0x18680, v21
	v_add_u32_e32 v16, 0x1c780, v21
	v_add_u32_e32 v13, 0x10480, v21
	ds_read_b32 v6, v6
	ds_read_b32 v8, v8
	ds_read_b32 v10, v10
	ds_read_b32 v12, v12
	ds_read_b32 v17, v13
	ds_read_b32 v14, v14
	ds_read_b32 v15, v15
	ds_read_b32 v16, v16
	v_add_f32_e32 v4, v4, v24
	s_waitcnt lgkmcnt(4)
	v_ashrrev_i32_e32 v13, 31, v12
	v_add_f32_e32 v4, v4, v6
	v_lshl_add_u64 v[12:13], v[12:13], 0, s[8:9]
	v_add_f32_e32 v4, v4, v8
	v_lshlrev_b64 v[12:13], 8, v[12:13]
	v_mul_f32_e32 v4, v4, v10
	v_lshl_add_u64 v[12:13], v[2:3], 0, v[12:13]
	global_store_dword v[12:13], v4, off sc1
	v_add_f32_e32 v4, 0, v5
	v_add_f32_e32 v4, v4, v7
	v_add_f32_e32 v4, v4, v9
	v_add_f32_e32 v4, v4, v11
	v_or_b32_e32 v7, 0xa00, v0
	s_waitcnt lgkmcnt(3)
	v_add_f32_e32 v4, v4, v17
	v_lshrrev_b32_e32 v7, 4, v7
	s_waitcnt lgkmcnt(2)
	v_add_f32_e32 v4, v4, v14
	v_and_b32_e32 v7, 0xbc, v7
	s_waitcnt lgkmcnt(1)
	v_add_f32_e32 v4, v4, v15
	v_mad_u32_u24 v10, v1, s0, v7
	s_waitcnt lgkmcnt(0)
	v_add_f32_e32 v5, v4, v16
	v_or_b32_e32 v4, 0x23980, v20
	v_or_b32_e32 v6, 0x23880, v20
	v_add_u32_e32 v8, 0x10400, v10
	v_add_u32_e32 v9, 0x14500, v10
	v_add_u32_e32 v12, 0x1c700, v10
	v_or_b32_e32 v13, 0x23900, v7
	v_add_u32_e32 v11, 0x18600, v10
	v_or_b32_e32 v7, 0x23800, v7
	ds_read_b32 v14, v4
	ds_read_b32 v4, v6
	ds_read_b32 v15, v8
	ds_read_b32 v16, v9
	ds_read_b32 v17, v11
	ds_read_b32 v12, v12
	ds_read_b32 v13, v13
	ds_read_b32 v6, v7
	ds_read2st64_b32 v[8:9], v10 offset1:65
	s_waitcnt lgkmcnt(8)
	v_mul_f32_e32 v7, v5, v14
	s_waitcnt lgkmcnt(7)
	v_ashrrev_i32_e32 v5, 31, v4
	v_lshl_add_u64 v[4:5], v[4:5], 0, s[8:9]
	ds_read2st64_b32 v[10:11], v10 offset0:130 offset1:195
	v_lshlrev_b64 v[4:5], 8, v[4:5]
	v_lshl_add_u64 v[4:5], v[2:3], 0, v[4:5]
	global_store_dword v[4:5], v7, off sc1
	s_waitcnt lgkmcnt(1)
	v_add_f32_e32 v4, 0, v8
	v_add_f32_e32 v4, v4, v9
	s_waitcnt lgkmcnt(0)
	v_add_f32_e32 v4, v4, v10
	v_add_f32_e32 v4, v4, v11
	v_add_f32_e32 v4, v4, v15
	v_add_f32_e32 v4, v4, v16
	v_add_f32_e32 v4, v4, v17
	v_add_f32_e32 v4, v4, v12
	v_ashrrev_i32_e32 v7, 31, v6
	v_mul_f32_e32 v8, v4, v13
	v_lshl_add_u64 v[4:5], v[6:7], 0, s[8:9]
	v_lshlrev_b64 v[4:5], 8, v[4:5]
	ds_read_b32 v6, v21 offset:33472
	ds_read_b32 v7, v21 offset:50112
	v_lshl_add_u64 v[4:5], v[2:3], 0, v[4:5]
	v_or_b32_e32 v0, 0xe00, v0
	global_store_dword v[4:5], v8, off sc1
	v_add_f32_e32 v4, 0, v22
	v_lshrrev_b32_e32 v0, 4, v0
	v_add_f32_e32 v4, v4, v23
	v_and_b32_e32 v11, 0xfc, v0
	s_waitcnt lgkmcnt(1)
	v_add_f32_e32 v4, v4, v6
	v_mad_u32_u24 v12, v1, s0, v11
	s_waitcnt lgkmcnt(0)
	v_add_f32_e32 v4, v4, v7
	v_add_u32_e32 v5, 0x104c0, v21
	v_add_u32_e32 v6, 0x145c0, v21
	v_add_u32_e32 v7, 0x186c0, v21
	v_add_u32_e32 v8, 0x1c7c0, v21
	v_or_b32_e32 v9, 0x239c0, v20
	v_or_b32_e32 v10, 0x238c0, v20
	v_add_u32_e32 v1, 0x10400, v12
	v_add_u32_e32 v13, 0x14500, v12
	ds_read_b32 v5, v5
	ds_read_b32 v6, v6
	ds_read_b32 v7, v7
	ds_read_b32 v8, v8
	ds_read_b32 v9, v9
	ds_read_b32 v0, v10
	ds_read_b32 v10, v1
	ds_read_b32 v13, v13
	s_waitcnt lgkmcnt(7)
	v_add_f32_e32 v1, v4, v5
	s_waitcnt lgkmcnt(6)
	v_add_f32_e32 v1, v1, v6
	s_waitcnt lgkmcnt(5)
	v_add_f32_e32 v1, v1, v7
	s_waitcnt lgkmcnt(4)
	v_add_f32_e32 v1, v1, v8
	ds_read2st64_b32 v[4:5], v12 offset1:65
	s_waitcnt lgkmcnt(4)
	v_mul_f32_e32 v8, v1, v9
	s_waitcnt lgkmcnt(3)
	v_ashrrev_i32_e32 v1, 31, v0
	v_lshl_add_u64 v[0:1], v[0:1], 0, s[8:9]
	ds_read2st64_b32 v[6:7], v12 offset0:130 offset1:195
	v_lshlrev_b64 v[0:1], 8, v[0:1]
	v_lshl_add_u64 v[0:1], v[2:3], 0, v[0:1]
	global_store_dword v[0:1], v8, off sc1
	s_waitcnt lgkmcnt(1)
	v_add_f32_e32 v0, 0, v4
	v_add_f32_e32 v0, v0, v5
	s_waitcnt lgkmcnt(0)
	v_add_f32_e32 v0, v0, v6
	v_add_f32_e32 v0, v0, v7
	v_add_f32_e32 v1, v0, v10
	v_add_u32_e32 v0, 0x18600, v12
	v_add_u32_e32 v4, 0x1c700, v12
	v_or_b32_e32 v5, 0x23900, v11
	v_or_b32_e32 v6, 0x23800, v11
	ds_read_b32 v7, v0
	ds_read_b32 v4, v4
	ds_read_b32 v5, v5
	ds_read_b32 v0, v6
	v_add_f32_e32 v1, v1, v13
	s_waitcnt lgkmcnt(3)
	v_add_f32_e32 v1, v1, v7
	s_waitcnt lgkmcnt(2)
	v_add_f32_e32 v1, v1, v4
	s_waitcnt lgkmcnt(1)
	v_mul_f32_e32 v4, v1, v5
	s_waitcnt lgkmcnt(0)
	v_ashrrev_i32_e32 v1, 31, v0
	v_lshl_add_u64 v[0:1], v[0:1], 0, s[8:9]
	v_lshlrev_b64 v[0:1], 8, v[0:1]
	v_lshl_add_u64 v[0:1], v[2:3], 0, v[0:1]
	global_store_dword v[0:1], v4, off sc1
	s_endpgm
